# P6 out-projection: accumulators initialised from the residual x (loaded right behind the previous unit's stores) instead of zero + epilogue load-add-store chain; epilogue is 32 plain stores
# baseline (speedup 1.0000x reference)
; #define LAS __attribute__((address_space(3)))
; DI const char* sptr(const char* p) { const unsigned long long v = (unsigned long long)p; const unsigned lo = __builtin_amdgcn_readfirstlane((unsigned)v), hi = __builtin_amdgcn_readfirstlane((unsigned)(v >> 32)); return (const char*)(((unsigned long long)hi << 32) | lo); }
; #define PG8_STAGE_B(bufoff, gbase) do { const char* sb_ = (const char*)(gbase); PG8_GLDS(sb_ + PG8_OPQ(voffB[0]), lds + (bufoff) + ldsw); PG8_GLDS(sb_ + PG8_OPQ(voffB[1]), lds + (bufoff) + ldsw + 8192); } while (0)
; #define PG8_STAGE_A(bufoff, gbase, o0, o1) do { const char* sb_ = (const char*)(gbase); PG8_GLDS(sb_ + PG8_OPQ(o0), lds + (bufoff) + ldsw); PG8_GLDS(sb_ + PG8_OPQ(o1), lds + (bufoff) + ldsw + 8192); } while (0)
; #define PG8_WAIT_V(n) asm volatile("s_waitcnt vmcnt(" #n ")" ::: "memory")
; template <class Epi, bool GATHER, bool EXPERT, bool FP8>
; DI void gemm_phase(LAS unsigned char* lds, const Gemm g, const StaticOrder& S, const Epi& E) {
;     ...
;     PG8_OFFS(coffA, cur.pm);
;     const char* cA = sptr((const char*)g.A + (GATHER ? (size_t)0 : (size_t)cur.pm * tstep));
;     const char* cB = sptr((const char*)g.Bt + (size_t)cur.e * g.estride + (size_t)cur.pn * tstep);
;     LAS unsigned char* est = g.estash + wid * 768;
;     if (Epi::STASH) E.prefetch(cur, wr, wc, lane, est);
;     LAS unsigned char* stash = g.stash + wid * 256;
;     PG8_STAGE_B(PG8_SB(0, 0), cB); PG8_STAGE_B(PG8_SB(0, 1), cB + hstep); PG8_STAGE_A(PG8_SA(0, 0), cA, coffA[0][0], coffA[0][1]); PG8_STAGE_A(PG8_SA(0, 1), cA, coffA[1][0], coffA[1][1]);
;     if (wr == 1) PG8_BAR;
;     PG8_WAIT_V(2); PG8_BAR;
;     PG8_STAGE_B(PG8_SB(1, 0), cB + kstep); PG8_STAGE_A(PG8_SA(1, 0), cA + kstep, coffA[0][0], coffA[0][1]); PG8_STAGE_B(PG8_SB(1, 1), cB + hstep + kstep);
;     PG8_WAIT_V(6); PG8_BAR;
;     DI void operator()(const f32x4 (&acc)[2][2][4][2], const Unit& u, int wr, int wc, int fr, int fq, const LAS unsigned char* st) const {
;         const int row0 = u.pm * BM + wr * 64 + fr, col0 = u.pn * BM + wc * 32 + 4 * fq;
;         f32x4 rb[4][4];
;     ...
;         EPS_LOAD(0); EPS_LOAD(1); EPS_LOAD(2);
; #pragma unroll
;         for (int ai = 0; ai < 2; ++ai)
; #pragma unroll
;             for (int m = 0; m < 4; ++m) { const int g = 4 * ai + m; const size_t off = (size_t)(row0 + ai * HALF + m * 16) * ldc + col0;
;                 if (g + 3 < 8) EPS_LOAD(g + 3);
.LBB0_783:
	v_mov_b32_e32 v130, v1
	v_mov_b32_e32 v131, 0
	s_waitcnt vmcnt(2)
	s_barrier
	s_mov_b64 s[68:69], 0x80
	v_lshl_add_u64 v[2:3], s[34:35], 0, v[130:131]
	v_lshl_add_u64 v[2:3], v[2:3], 0, s[68:69]
	s_add_i32 m0, s29, 0x18000
	v_mov_b32_e32 v130, v142
	global_load_lds_dwordx4 v[2:3], off
	s_add_i32 m0, s29, 0x1a000
	v_lshl_add_u64 v[2:3], s[34:35], 0, v[130:131]
	v_lshl_add_u64 v[2:3], v[2:3], 0, s[68:69]
	v_mov_b32_e32 v130, v143
	global_load_lds_dwordx4 v[2:3], off
	s_add_i32 s47, s29, 0x8000
	v_lshl_add_u64 v[2:3], s[30:31], 0, v[130:131]
	s_lshl_b32 s3, s3, 5
	v_lshl_add_u64 v[2:3], v[2:3], 0, s[68:69]
	s_mov_b32 m0, s47
	v_mov_b32_e32 v130, v145
	s_and_b32 s46, s3, 0x60
	global_load_lds_dwordx4 v[2:3], off
	s_add_i32 s48, s29, 0xa000
	v_lshl_add_u64 v[2:3], s[30:31], 0, v[130:131]
	s_lshl_b32 s45, s1, 6
	s_lshl_b32 s1, s1, 13
	s_lshl_b32 s3, s46, 7
	v_lshl_add_u64 v[2:3], v[2:3], 0, s[68:69]
	s_mov_b32 m0, s48
	s_add_u32 s10, s34, 0x80080
	global_load_lds_dwordx4 v[2:3], off
	v_mov_b32_e32 v2, v1
	s_addc_u32 s11, s35, 0
	s_add_i32 m0, s29, 0x1c000
	s_sext_i32_i8 s54, s0
	global_load_lds_dwordx4 v2, s[10:11]
	v_mov_b32_e32 v2, v142
	s_add_i32 m0, s29, 0x1e000
	v_lshlrev_b32_e32 v3, 6, v0
	global_load_lds_dwordx4 v2, s[10:11]
	v_and_b32_e32 v2, 48, v0
	s_movk_i32 s0, 0x3c0
	v_and_or_b32 v2, v3, s0, v2
	v_lshlrev_b32_e32 v3, 2, v0
	v_and_b32_e32 v3, 32, v3
	s_waitcnt vmcnt(6)
	s_cmpk_lt_u32 s2, 0x100
	v_bitop3_b32 v4, v2, s1, v3 bitop3:0xde
	s_waitcnt vmcnt(0)
	v_bitop3_b32 v147, s3, v2, v3 bitop3:0xf6
	s_cselect_b64 s[72:73], -1, 0
	v_readlane_b32 s0, v254, 2
	s_add_i32 s50, 0, 0x10000
	s_add_i32 s51, 0, 0x14000
	s_ashr_i32 s49, s0, 31
	v_mov_b64_e32 v[132:133], 0x400
	v_mov_b64_e32 v[134:135], 0x3ff
	v_add_u32_e32 v148, s50, v147
	v_add_u32_e32 v149, s51, v147
	v_add_u32_e32 v150, 0, v4
	s_mov_b64 s[74:75], 0x100000
	s_mov_b64 s[76:77], 0x120000
	s_mov_b64 s[16:17], 0x140000
	s_mov_b32 s52, 0x140000
	s_mov_b64 s[18:19], 0x160000
	s_mov_b32 s53, 0x160000
	s_barrier
	v_readlane_b32 vcc_lo, v254, 3
	v_readlane_b32 vcc_hi, v254, 4
	s_lshl_b32 s0, s28, 8
	s_add_i32 s0, s0, s45
	v_and_or_b32 v140, v224, 15, s0
	s_lshl_b32 s0, s54, 8
	v_ashrrev_i32_e32 v136, 2, v224
	s_or_b32 s0, s0, s46
	v_and_b32_e32 v136, -4, v136
	v_add_u32_e32 v136, s0, v136
	v_lshlrev_b32_e32 v140, 13, v140
	v_lshl_add_u32 v130, v136, 2, v140
	s_mov_b32 s0, vcc_lo
	s_mov_b32 s1, vcc_hi
	global_load_dwordx4 v[126:129], v130, s[0:1]
	global_load_dwordx4 v[122:125], v130, s[0:1] offset:64
	global_load_dwordx4 v[106:109], v130, s[0:1] offset:512
	global_load_dwordx4 v[102:105], v130, s[0:1] offset:576
	s_add_u32 s0, vcc_lo, 0x20000
	s_addc_u32 s1, vcc_hi, 0
	global_load_dwordx4 v[118:121], v130, s[0:1]
	global_load_dwordx4 v[114:117], v130, s[0:1] offset:64
	global_load_dwordx4 v[98:101], v130, s[0:1] offset:512
	global_load_dwordx4 v[94:97], v130, s[0:1] offset:576
	s_add_u32 s0, vcc_lo, 0x40000
	s_addc_u32 s1, vcc_hi, 0
	global_load_dwordx4 v[110:113], v130, s[0:1]
	global_load_dwordx4 v[90:93], v130, s[0:1] offset:64
	global_load_dwordx4 v[86:89], v130, s[0:1] offset:512
	global_load_dwordx4 v[78:81], v130, s[0:1] offset:576
	s_add_u32 s0, vcc_lo, 0x60000
	s_addc_u32 s1, vcc_hi, 0
	global_load_dwordx4 v[82:85], v130, s[0:1]
	global_load_dwordx4 v[74:77], v130, s[0:1] offset:64
	global_load_dwordx4 v[70:73], v130, s[0:1] offset:512
	global_load_dwordx4 v[66:69], v130, s[0:1] offset:576
	s_add_u32 s0, vcc_lo, 0x100000
	s_addc_u32 s1, vcc_hi, 0
	global_load_dwordx4 v[62:65], v130, s[0:1]
	global_load_dwordx4 v[58:61], v130, s[0:1] offset:64
	global_load_dwordx4 v[46:49], v130, s[0:1] offset:512
	global_load_dwordx4 v[38:41], v130, s[0:1] offset:576
	s_add_u32 s0, vcc_lo, 0x120000
	s_addc_u32 s1, vcc_hi, 0
	global_load_dwordx4 v[54:57], v130, s[0:1]
	global_load_dwordx4 v[50:53], v130, s[0:1] offset:64
	global_load_dwordx4 v[30:33], v130, s[0:1] offset:512
	global_load_dwordx4 v[26:29], v130, s[0:1] offset:576
	s_add_u32 s0, vcc_lo, 0x140000
	s_addc_u32 s1, vcc_hi, 0
	global_load_dwordx4 v[42:45], v130, s[0:1]
	global_load_dwordx4 v[34:37], v130, s[0:1] offset:64
	global_load_dwordx4 v[18:21], v130, s[0:1] offset:512
	global_load_dwordx4 v[14:17], v130, s[0:1] offset:576
	s_add_u32 s0, vcc_lo, 0x160000
	s_addc_u32 s1, vcc_hi, 0
	global_load_dwordx4 v[22:25], v130, s[0:1]
	global_load_dwordx4 v[10:13], v130, s[0:1] offset:64
	global_load_dwordx4 v[6:9], v130, s[0:1] offset:512
	global_load_dwordx4 v[2:5], v130, s[0:1] offset:576
	s_branch .LBB0_786

; DI const char* sptr(const char* p) { const unsigned long long v = (unsigned long long)p; const unsigned lo = __builtin_amdgcn_readfirstlane((unsigned)v), hi = __builtin_amdgcn_readfirstlane((unsigned)(v >> 32)); return (const char*)(((unsigned long long)hi << 32) | lo); }
;     DI bool next(int i, Unit& u) const {
;         const long L = (long)i * G + c; if (L >= nwg) return false;
;         int wgid = (int)L; { const int q = nwg / NXCD, r = nwg % NXCD, xcd = wgid % NXCD, off = wgid / NXCD; wgid = (xcd < r ? xcd * (q + 1) : r * (q + 1) + (xcd - r) * q) + off; }
;         const int nig = WGM * nN, gid = wgid / nig, fm = gid * WGM, gsz = (nM - fm) < WGM ? (nM - fm) : WGM;
;         u.pm = fm + ((wgid % nig) % gsz); u.pn = (wgid % nig) / gsz; u.e = 0; return true;
; template <class Epi, bool GATHER, bool EXPERT, bool FP8>
; DI void gemm_phase(LAS unsigned char* lds, const Gemm g, const StaticOrder& S, const Epi& E) {
;     ...
;     for (;;) {
;         const bool has_next = S.next(ui + 1, nxt);
;         if (EXPERT) nxt.e = has_next ? __builtin_amdgcn_readfirstlane(g.tile_e[nxt.pm]) : 0;
;         const char* nA = sptr(has_next ? (const char*)g.A + (GATHER ? (size_t)0 : (size_t)nxt.pm * tstep) : cA);
;         const char* nB = sptr(has_next ? (const char*)g.Bt + (size_t)nxt.e * g.estride + (size_t)nxt.pn * tstep : cB);
.LBB0_791:
	s_ashr_i32 s0, s20, 3
	s_add_i32 s0, s22, s0
	s_ashr_i32 s1, s0, 31
	s_lshr_b32 s1, s1, 26
	s_add_i32 s1, s0, s1
	s_ashr_i32 s20, s1, 6
	s_lshl_b32 s21, s20, 3
	s_sub_i32 s20, 0x80, s21
	s_min_i32 s22, s20, 8
	s_abs_i32 s20, s22
	v_cvt_f32_u32_e32 v130, s20
	s_sub_i32 s24, 0, s20
	s_andn2_b32 s1, s1, 63
	s_sub_i32 s0, s0, s1
	v_rcp_iflag_f32_e32 v130, v130
	s_abs_i32 s1, s0
	s_xor_b32 s23, s0, s22
	s_ashr_i32 s23, s23, 31
	v_mul_f32_e32 v130, 0x4f7ffffe, v130
	v_cvt_u32_f32_e32 v130, v130
	s_nop 0
	v_readfirstlane_b32 s25, v130
	s_mul_i32 s24, s24, s25
	s_mul_hi_u32 s24, s25, s24
	s_add_i32 s25, s25, s24
	s_mul_hi_u32 s24, s1, s25
	s_mul_i32 s25, s24, s20
	s_sub_i32 s1, s1, s25
	s_add_i32 s26, s24, 1
	s_sub_i32 s25, s1, s20
	s_cmp_ge_u32 s1, s20
	s_cselect_b32 s24, s26, s24
	s_cselect_b32 s1, s25, s1
	s_add_i32 s25, s24, 1
	s_cmp_ge_u32 s1, s20
	s_cselect_b32 s1, s25, s24
	s_xor_b32 s1, s1, s23
	s_sub_i32 s20, s1, s23
	s_mul_i32 s1, s20, s22
	s_sub_i32 s0, s0, s1
	s_add_i32 s22, s21, s0
.LBB0_792:
	s_ashr_i32 s23, s22, 31
	s_lshl_b64 s[0:1], s[22:23], 20
	s_add_u32 s21, s37, s0
	s_addc_u32 s23, s38, s1
	s_and_b64 s[0:1], s[60:61], exec
	s_cselect_b32 s24, s21, s30
	s_cselect_b32 s25, s23, s31
	s_ashr_i32 s21, s20, 31
	s_lshl_b64 s[0:1], s[20:21], 20
	s_add_u32 s21, s33, s0
	s_addc_u32 s23, s39, s1
	s_and_b64 s[0:1], s[60:61], exec
	s_cselect_b32 s26, s21, s34
	s_cselect_b32 s27, s23, s35
	s_add_u32 s21, s34, 0x100
	.p2align 8
	s_addc_u32 s23, s35, 0
	s_add_u32 s30, s30, 0x80
	s_addc_u32 s31, s31, 0
	s_mov_b32 s55, -2
	s_waitcnt vmcnt(0)

; #define EPS_LOAD(g_) do { const size_t off_ = (size_t)(row0 + ((g_) >> 2) * HALF + ((g_) & 3) * 16) * ldc + col0; \
;             _Pragma("unroll") for (int bj = 0; bj < 2; ++bj) _Pragma("unroll") for (int n = 0; n < 2; ++n) rb[(g_) & 3][2 * bj + n] = *(const f32x4*)(base + off_ + bj * HALF + n * 16); } while (0)
;     DI void operator()(const f32x4 (&acc)[2][2][4][2], const Unit& u, int wr, int wc, int fr, int fq, const LAS unsigned char* st) const {
;         const int row0 = u.pm * BM + wr * 64 + fr, col0 = u.pn * BM + wc * 32 + 4 * fq;
;         f32x4 rb[4][4];
;     ...
;         EPS_LOAD(0); EPS_LOAD(1); EPS_LOAD(2);
; #pragma unroll
;         for (int ai = 0; ai < 2; ++ai)
; #pragma unroll
;             for (int m = 0; m < 4; ++m) { const int g = 4 * ai + m; const size_t off = (size_t)(row0 + ai * HALF + m * 16) * ldc + col0;
;                 if (g + 3 < 8) EPS_LOAD(g + 3);
; #pragma unroll
;                 for (int bj = 0; bj < 2; ++bj)
; #pragma unroll
;                     for (int n = 0; n < 2; ++n) *(f32x4*)(C + off + bj * HALF + n * 16) = rb[g & 3][2 * bj + n] + acc[ai][bj][m][n]; }
.LBB0_796:
	s_lshl_b32 s0, s28, 8
	s_add_i32 s0, s0, s45
	v_and_or_b32 v140, v224, 15, s0
	s_lshl_b32 s0, s54, 8
	v_ashrrev_i32_e32 v136, 2, v224
	s_or_b32 s0, s0, s46
	v_and_b32_e32 v136, -4, v136
	v_add_u32_e32 v136, s0, v136
	v_lshlrev_b32_e32 v140, 13, v140
	v_lshl_add_u32 v130, v136, 2, v140
	s_mov_b32 s0, s92
	s_mov_b32 s1, s93
	global_store_dwordx4 v130, v[126:129], s[0:1]
	global_store_dwordx4 v130, v[122:125], s[0:1] offset:64
	global_store_dwordx4 v130, v[106:109], s[0:1] offset:512
	global_store_dwordx4 v130, v[102:105], s[0:1] offset:576
	s_add_u32 s0, s92, 0x20000
	s_addc_u32 s1, s93, 0
	global_store_dwordx4 v130, v[118:121], s[0:1]
	global_store_dwordx4 v130, v[114:117], s[0:1] offset:64
	global_store_dwordx4 v130, v[98:101], s[0:1] offset:512
	global_store_dwordx4 v130, v[94:97], s[0:1] offset:576
	s_add_u32 s0, s92, 0x40000
	s_addc_u32 s1, s93, 0
	global_store_dwordx4 v130, v[110:113], s[0:1]
	global_store_dwordx4 v130, v[90:93], s[0:1] offset:64
	global_store_dwordx4 v130, v[86:89], s[0:1] offset:512
	global_store_dwordx4 v130, v[78:81], s[0:1] offset:576
	s_add_u32 s0, s92, 0x60000
	s_addc_u32 s1, s93, 0
	global_store_dwordx4 v130, v[82:85], s[0:1]
	global_store_dwordx4 v130, v[74:77], s[0:1] offset:64
	global_store_dwordx4 v130, v[70:73], s[0:1] offset:512
	global_store_dwordx4 v130, v[66:69], s[0:1] offset:576
	s_add_u32 s0, s92, 0x100000
	s_addc_u32 s1, s93, 0
	global_store_dwordx4 v130, v[62:65], s[0:1]
	global_store_dwordx4 v130, v[58:61], s[0:1] offset:64
	global_store_dwordx4 v130, v[46:49], s[0:1] offset:512
	global_store_dwordx4 v130, v[38:41], s[0:1] offset:576
	s_add_u32 s0, s92, 0x120000
	s_addc_u32 s1, s93, 0
	global_store_dwordx4 v130, v[54:57], s[0:1]
	global_store_dwordx4 v130, v[50:53], s[0:1] offset:64
	global_store_dwordx4 v130, v[30:33], s[0:1] offset:512
	global_store_dwordx4 v130, v[26:29], s[0:1] offset:576
	s_add_u32 s0, s92, 0x140000
	s_addc_u32 s1, s93, 0
	global_store_dwordx4 v130, v[42:45], s[0:1]
	global_store_dwordx4 v130, v[34:37], s[0:1] offset:64
	global_store_dwordx4 v130, v[18:21], s[0:1] offset:512
	global_store_dwordx4 v130, v[14:17], s[0:1] offset:576
	s_add_u32 s0, s92, 0x160000
	s_addc_u32 s1, s93, 0
	global_store_dwordx4 v130, v[22:25], s[0:1]
	global_store_dwordx4 v130, v[10:13], s[0:1] offset:64
	global_store_dwordx4 v130, v[6:9], s[0:1] offset:512
	global_store_dwordx4 v130, v[2:5], s[0:1] offset:576
	s_and_b64 vcc, exec, s[60:61]
	s_cbranch_vccz .Lp6_noxload
	v_readlane_b32 vcc_lo, v254, 3
	v_readlane_b32 vcc_hi, v254, 4
	s_lshl_b32 s0, s22, 8
	s_add_i32 s0, s0, s45
	v_and_or_b32 v140, v224, 15, s0
	s_lshl_b32 s0, s20, 8
	v_ashrrev_i32_e32 v136, 2, v224
	s_or_b32 s0, s0, s46
	v_and_b32_e32 v136, -4, v136
	v_add_u32_e32 v136, s0, v136
	v_lshlrev_b32_e32 v140, 13, v140
	v_lshl_add_u32 v130, v136, 2, v140
	s_mov_b32 s0, vcc_lo
	s_mov_b32 s1, vcc_hi
	global_load_dwordx4 v[126:129], v130, s[0:1]
	global_load_dwordx4 v[122:125], v130, s[0:1] offset:64
	global_load_dwordx4 v[106:109], v130, s[0:1] offset:512
	global_load_dwordx4 v[102:105], v130, s[0:1] offset:576
	s_add_u32 s0, vcc_lo, 0x20000
	s_addc_u32 s1, vcc_hi, 0
	global_load_dwordx4 v[118:121], v130, s[0:1]
	global_load_dwordx4 v[114:117], v130, s[0:1] offset:64
	global_load_dwordx4 v[98:101], v130, s[0:1] offset:512
	global_load_dwordx4 v[94:97], v130, s[0:1] offset:576
	s_add_u32 s0, vcc_lo, 0x40000
	s_addc_u32 s1, vcc_hi, 0
	global_load_dwordx4 v[110:113], v130, s[0:1]
	global_load_dwordx4 v[90:93], v130, s[0:1] offset:64
	global_load_dwordx4 v[86:89], v130, s[0:1] offset:512
	global_load_dwordx4 v[78:81], v130, s[0:1] offset:576
	s_add_u32 s0, vcc_lo, 0x60000
	s_addc_u32 s1, vcc_hi, 0
	global_load_dwordx4 v[82:85], v130, s[0:1]
	global_load_dwordx4 v[74:77], v130, s[0:1] offset:64
	global_load_dwordx4 v[70:73], v130, s[0:1] offset:512
	global_load_dwordx4 v[66:69], v130, s[0:1] offset:576
	s_add_u32 s0, vcc_lo, 0x100000
	s_addc_u32 s1, vcc_hi, 0
	global_load_dwordx4 v[62:65], v130, s[0:1]
	global_load_dwordx4 v[58:61], v130, s[0:1] offset:64
	global_load_dwordx4 v[46:49], v130, s[0:1] offset:512
	global_load_dwordx4 v[38:41], v130, s[0:1] offset:576
	s_add_u32 s0, vcc_lo, 0x120000
	s_addc_u32 s1, vcc_hi, 0
	global_load_dwordx4 v[54:57], v130, s[0:1]
	global_load_dwordx4 v[50:53], v130, s[0:1] offset:64
	global_load_dwordx4 v[30:33], v130, s[0:1] offset:512
	global_load_dwordx4 v[26:29], v130, s[0:1] offset:576
	s_add_u32 s0, vcc_lo, 0x140000
	s_addc_u32 s1, vcc_hi, 0
	global_load_dwordx4 v[42:45], v130, s[0:1]
	global_load_dwordx4 v[34:37], v130, s[0:1] offset:64
	global_load_dwordx4 v[18:21], v130, s[0:1] offset:512
	global_load_dwordx4 v[14:17], v130, s[0:1] offset:576
	s_add_u32 s0, vcc_lo, 0x160000
	s_addc_u32 s1, vcc_hi, 0
	global_load_dwordx4 v[22:25], v130, s[0:1]
	global_load_dwordx4 v[10:13], v130, s[0:1] offset:64
	global_load_dwordx4 v[6:9], v130, s[0:1] offset:512
	global_load_dwordx4 v[2:5], v130, s[0:1] offset:576
.Lp6_noxload:
	v_readlane_b32 s2, v254, 5
	v_readlane_b32 s3, v254, 6
	v_readlane_b32 s4, v254, 7
	v_readlane_b32 s5, v254, 8
	v_readlane_b32 s6, v254, 9
	v_readlane_b32 s7, v254, 10
	v_readlane_b32 s8, v254, 11
	v_readlane_b32 s9, v254, 12
	v_readlane_b32 s10, v254, 13
	v_readlane_b32 s11, v254, 14
	v_readlane_b32 s12, v254, 15
	v_readlane_b32 s13, v254, 16
	v_readlane_b32 s14, v254, 17
	v_readlane_b32 s15, v254, 18
	s_mov_b64 s[0:1], -1
	s_andn2_b64 vcc, exec, s[60:61]
	s_cbranch_vccnz .LBB0_785
	s_andn2_b64 vcc, exec, s[64:65]
	s_cbranch_vccnz .LBB0_784
	s_barrier
	s_branch .LBB0_784
